# baseline (speedup 1.0000x reference)
_Z16sum_layer_kernelPKfS0_Pf:
	s_load_dwordx4 s[4:7], s[0:1], 0x0
	s_load_dwordx2 s[8:9], s[0:1], 0x10
	v_lshrrev_b32_e32 v42, 6, v0
	v_bfe_u32 v41, v0, 5, 1
	v_and_b32_e32 v40, 31, v0
	v_readfirstlane_b32 s23, v42
	v_and_b32_e32 v43, 7, v0
	v_bfe_u32 v44, v0, 3, 3
	s_lshl_b32 s3, s2, 12
	s_lshl_b32 s19, s2, 7
	s_lshl_b32 s23, s23, 12
	v_lshlrev_b32_e32 v1, 11, v41
	v_lshl_or_b32 v1, v40, 2, v1
	s_mov_b32 m0, s23
	v_lshrrev_b32_e32 v46, 1, v44
	v_xor_b32_e32 v46, v43, v46
	v_lshlrev_b32_e32 v46, 4, v46
	v_lshl_add_u32 v35, v44, 16, v46
	v_lshl_add_u32 v35, v42, 21, v35
	v_add_u32_e32 v35, s19, v35
	v_xor_b32_e32 v86, 64, v35
	s_mov_b32 s20, 0x7fc00
	s_mov_b32 s21, 0xff800
	s_mov_b32 s22, 0x17f400
	s_mov_b32 s14, 0x200000
	s_mov_b32 s15, 0x20000
	v_and_b32_e32 v45, 63, v0
	v_lshlrev_b32_e32 v37, 4, v45
	s_add_u32 s54, s23, 0x4000
	s_waitcnt lgkmcnt(0)
	s_mov_b32 s12, s6
	s_and_b32 s13, s7, 0xffff
	s_and_b32 s5, s5, 0xffff
	s_mov_b32 s6, 0x800000
	s_mov_b32 s7, s15
	s_mov_b32 m0, s54
	s_nop 0
	buffer_load_dwordx4 v37, s[12:15], s3 offen nt lds
	buffer_load_dwordx4 v37, s[12:15], s3 offen offset:1024 nt lds
	buffer_load_dwordx4 v37, s[12:15], s3 offen offset:2048 nt lds
	buffer_load_dwordx4 v37, s[12:15], s3 offen offset:3072 nt lds
	s_mov_b32 m0, s23
	s_nop 0
	buffer_load_dwordx4 v35, s[4:7], 0 offen nt lds
	buffer_load_dwordx4 v86, s[4:7], s20 offen offset:1024 nt lds
	buffer_load_dwordx4 v35, s[4:7], s21 offen offset:2048 nt lds
	buffer_load_dwordx4 v86, s[4:7], s22 offen offset:3072 nt lds
	v_and_b32_e32 v45, 63, v0
	v_lshlrev_b32_e32 v36, 2, v40
	v_lshl_add_u32 v36, v41, 18, v36
	v_lshl_add_u32 v36, v42, 21, v36
	v_add_u32_e32 v36, s19, v36
	v_bfe_u32 v47, v40, 1, 3
	v_lshlrev_b32_e32 v39, 2, v41
	v_xor_b32_e32 v39, v39, v47
	v_lshlrev_b32_e32 v39, 4, v39
	v_lshl_add_u32 v39, v40, 7, v39
	v_lshl_add_u32 v39, v42, 12, v39
	v_xor_b32_e32 v81, 16, v39
	v_xor_b32_e32 v82, 32, v39
	v_xor_b32_e32 v83, 48, v39
	v_cmp_gt_u32_e32 vcc, 32, v45
	v_mov_b32_e32 v34, 0xc1600000
	v_mov_b32_e32 v84, 0x3fb8aa3b
	v_mov_b32_e32 v85, 0x3f317218
	v_lshlrev_b32_e32 v36, 4, v43
	v_lshl_add_u32 v36, v44, 16, v36
	v_lshl_add_u32 v36, v42, 21, v36
	v_add_u32_e32 v36, s19, v36
	v_mul_u32_u24_e32 v37, 0x1200, v42
	v_add_u32_e32 v37, 0x8000, v37
	v_mul_u32_u24_e32 v38, 0x90, v40
	v_lshlrev_b32_e32 v87, 4, v41
	v_add3_u32 v38, v37, v38, v87
	v_mul_u32_u24_e32 v87, 0x90, v44
	v_lshlrev_b32_e32 v46, 4, v43
	v_add3_u32 v87, v37, v87, v46
	s_mov_b32 s24, 0x80000
	s_mov_b32 s25, 0x100000
	s_mov_b32 s26, 0x180000
	s_and_b32 s9, s9, 0xffff
	s_mov_b32 s10, s6
	s_mov_b32 s11, s15
	v_lshl_add_u32 v0, v42, 12, v1
	v_add_u32_e32 v0, 0x4000, v0
	v_add_u32_e32 v1, 0x400, v0
	s_waitcnt vmcnt(4)
	ds_read2_b32 v[18:19], v0 offset0:0 offset1:32
	ds_read2_b32 v[20:21], v0 offset0:64 offset1:96
	ds_read2_b32 v[22:23], v0 offset0:128 offset1:160
	ds_read2_b32 v[24:25], v0 offset0:192 offset1:224
	ds_read2_b32 v[26:27], v1 offset0:0 offset1:32
	ds_read2_b32 v[28:29], v1 offset0:64 offset1:96
	ds_read2_b32 v[30:31], v1 offset0:128 offset1:160
	ds_read2_b32 v[32:33], v1 offset0:192 offset1:224
	s_waitcnt lgkmcnt(0)
	v_max3_f32 v48, v18, v19, v20
	v_max3_f32 v50, v21, v22, v23
	v_max3_f32 v48, v48, v24, v25
	v_max3_f32 v50, v50, v26, v27
	v_max3_f32 v48, v48, v28, v29
	v_max3_f32 v50, v50, v30, v31
	v_max3_f32 v48, v48, v32, v33
	v_max_f32_e32 v48, v48, v50
	v_mov_b32_e32 v50, v48
	s_nop 1
	v_permlane32_swap_b32_e32 v48, v50
	v_max_f32_e32 v48, v48, v50
	v_fmamk_f32 v48, v48, 0x3fb8aa3b, v34
	v_pk_fma_f32 v[18:19], v[18:19], v[84:85], v[48:49] op_sel_hi:[1,0,0] neg_lo:[0,0,1] neg_hi:[0,0,1]
	v_exp_f32_e32 v18, v18
	v_exp_f32_e32 v19, v19
	v_pk_fma_f32 v[20:21], v[20:21], v[84:85], v[48:49] op_sel_hi:[1,0,0] neg_lo:[0,0,1] neg_hi:[0,0,1]
	v_exp_f32_e32 v20, v20
	v_exp_f32_e32 v21, v21
	v_pk_fma_f32 v[22:23], v[22:23], v[84:85], v[48:49] op_sel_hi:[1,0,0] neg_lo:[0,0,1] neg_hi:[0,0,1]
	v_exp_f32_e32 v22, v22
	v_exp_f32_e32 v23, v23
	v_pk_fma_f32 v[24:25], v[24:25], v[84:85], v[48:49] op_sel_hi:[1,0,0] neg_lo:[0,0,1] neg_hi:[0,0,1]
	v_exp_f32_e32 v24, v24
	v_exp_f32_e32 v25, v25
	v_pk_fma_f32 v[26:27], v[26:27], v[84:85], v[48:49] op_sel_hi:[1,0,0] neg_lo:[0,0,1] neg_hi:[0,0,1]
	v_exp_f32_e32 v26, v26
	v_exp_f32_e32 v27, v27
	v_pk_fma_f32 v[28:29], v[28:29], v[84:85], v[48:49] op_sel_hi:[1,0,0] neg_lo:[0,0,1] neg_hi:[0,0,1]
	v_exp_f32_e32 v28, v28
	v_exp_f32_e32 v29, v29
	v_pk_fma_f32 v[30:31], v[30:31], v[84:85], v[48:49] op_sel_hi:[1,0,0] neg_lo:[0,0,1] neg_hi:[0,0,1]
	v_exp_f32_e32 v30, v30
	v_exp_f32_e32 v31, v31
	v_pk_fma_f32 v[32:33], v[32:33], v[84:85], v[48:49] op_sel_hi:[1,0,0] neg_lo:[0,0,1] neg_hi:[0,0,1]
	v_exp_f32_e32 v32, v32
	v_exp_f32_e32 v33, v33
	v_pk_add_f32 v[56:57], v[18:19], v[20:21]
	v_pk_add_f32 v[58:59], v[22:23], v[24:25]
	v_pk_add_f32 v[60:61], v[26:27], v[28:29]
	v_pk_add_f32 v[62:63], v[30:31], v[32:33]
	v_pk_add_f32 v[56:57], v[56:57], v[58:59]
	v_pk_add_f32 v[60:61], v[60:61], v[62:63]
	v_pk_add_f32 v[56:57], v[56:57], v[60:61]
	v_add_f32_e32 v50, v56, v57
	v_mov_b32_e32 v51, v50
	s_nop 1
	v_permlane32_swap_b32_e32 v50, v51
	v_add_f32_e32 v50, v50, v51
	v_log_f32_e32 v50, v50
	v_cvt_pk_f16_f32 v40, v18, v19
	v_cvt_pk_f16_f32 v41, v20, v21
	v_cvt_pk_f16_f32 v42, v22, v23
	v_cvt_pk_f16_f32 v43, v24, v25
	v_cvt_pk_f16_f32 v44, v26, v27
	v_cvt_pk_f16_f32 v45, v28, v29
	v_cvt_pk_f16_f32 v46, v30, v31
	v_cvt_pk_f16_f32 v47, v32, v33
	v_add_f32_e32 v50, 0x41600000, v50
	v_mul_f32_e32 v50, 0xbf317218, v50
	v_cndmask_b32_e64 v51, v50, 1.0, vcc
	s_waitcnt vmcnt(0)
	ds_read_b128 v[2:5], v39
	ds_read_b128 v[6:9], v81
	ds_read_b128 v[10:13], v82
	ds_read_b128 v[14:17], v83
	s_waitcnt lgkmcnt(2)
	v_max3_f32 v52, v2, v3, v4
	v_max3_f32 v53, v5, v6, v7
	v_max_f32_e32 v52, v52, v8
	v_max_f32_e32 v53, v53, v9
	s_waitcnt lgkmcnt(0)
	v_max3_f32 v52, v52, v10, v11
	v_max3_f32 v53, v53, v12, v13
	v_max3_f32 v52, v52, v14, v15
	v_max3_f32 v53, v53, v16, v17
	v_max_f32_e32 v52, v52, v53
	v_mov_b32_e32 v53, v52
	s_nop 1
	v_permlane32_swap_b32_e32 v52, v53
	v_max_f32_e32 v52, v52, v53
	v_cndmask_b32_e32 v54, 1.0, v52, vcc
	v_fmamk_f32 v48, v52, 0x3fb8aa3b, v34
	v_pk_fma_f32 v[2:3], v[2:3], v[84:85], v[48:49] op_sel_hi:[1,0,0] neg_lo:[0,0,1] neg_hi:[0,0,1]
	v_mfma_f32_32x32x2_f32 v[64:79], v51, v54, 0
	v_exp_f32_e32 v2, v2
	v_exp_f32_e32 v3, v3
	v_pk_fma_f32 v[4:5], v[4:5], v[84:85], v[48:49] op_sel_hi:[1,0,0] neg_lo:[0,0,1] neg_hi:[0,0,1]
	v_exp_f32_e32 v4, v4
	v_exp_f32_e32 v5, v5
	v_pk_fma_f32 v[6:7], v[6:7], v[84:85], v[48:49] op_sel_hi:[1,0,0] neg_lo:[0,0,1] neg_hi:[0,0,1]
	v_exp_f32_e32 v6, v6
	v_exp_f32_e32 v7, v7
	v_pk_fma_f32 v[8:9], v[8:9], v[84:85], v[48:49] op_sel_hi:[1,0,0] neg_lo:[0,0,1] neg_hi:[0,0,1]
	v_exp_f32_e32 v8, v8
	v_exp_f32_e32 v9, v9
	v_pk_fma_f32 v[10:11], v[10:11], v[84:85], v[48:49] op_sel_hi:[1,0,0] neg_lo:[0,0,1] neg_hi:[0,0,1]
	v_exp_f32_e32 v10, v10
	v_cvt_pk_f16_f32 v56, v2, v3
	v_cvt_pk_f16_f32 v57, v4, v5
	v_cvt_pk_f16_f32 v58, v6, v7
	v_cvt_pk_f16_f32 v59, v8, v9
	v_exp_f32_e32 v11, v11
	v_pk_fma_f32 v[12:13], v[12:13], v[84:85], v[48:49] op_sel_hi:[1,0,0] neg_lo:[0,0,1] neg_hi:[0,0,1]
	v_exp_f32_e32 v12, v12
	v_mfma_f32_32x32x16_f16 v[18:33], v[40:43], v[56:59], 0
	v_exp_f32_e32 v13, v13
	v_pk_fma_f32 v[14:15], v[14:15], v[84:85], v[48:49] op_sel_hi:[1,0,0] neg_lo:[0,0,1] neg_hi:[0,0,1]
	v_exp_f32_e32 v14, v14
	v_exp_f32_e32 v15, v15
	v_pk_fma_f32 v[16:17], v[16:17], v[84:85], v[48:49] op_sel_hi:[1,0,0] neg_lo:[0,0,1] neg_hi:[0,0,1]
	v_exp_f32_e32 v16, v16
	v_exp_f32_e32 v17, v17
	v_cvt_pk_f16_f32 v60, v10, v11
	v_cvt_pk_f16_f32 v61, v12, v13
	v_cvt_pk_f16_f32 v62, v14, v15
	v_cvt_pk_f16_f32 v63, v16, v17
	s_nop 1
	v_mfma_f32_32x32x16_f16 v[18:33], v[44:47], v[60:63], v[18:33]
	s_nop 11
	v_log_f32_e32 v18, v18
	v_log_f32_e32 v19, v19
	v_log_f32_e32 v20, v20
	v_log_f32_e32 v21, v21
	v_log_f32_e32 v22, v22
	v_log_f32_e32 v23, v23
	v_log_f32_e32 v24, v24
	v_log_f32_e32 v25, v25
	v_pk_fma_f32 v[64:65], v[18:19], v[84:85], v[64:65] op_sel:[0,1,0] op_sel_hi:[1,1,1]
	v_log_f32_e32 v26, v26
	v_log_f32_e32 v27, v27
	v_pk_fma_f32 v[66:67], v[20:21], v[84:85], v[66:67] op_sel:[0,1,0] op_sel_hi:[1,1,1]
	ds_write_b128 v38, v[64:67]
	v_log_f32_e32 v28, v28
	v_log_f32_e32 v29, v29
	v_pk_fma_f32 v[68:69], v[22:23], v[84:85], v[68:69] op_sel:[0,1,0] op_sel_hi:[1,1,1]
	v_log_f32_e32 v30, v30
	v_log_f32_e32 v31, v31
	v_pk_fma_f32 v[70:71], v[24:25], v[84:85], v[70:71] op_sel:[0,1,0] op_sel_hi:[1,1,1]
	ds_write_b128 v38, v[68:71] offset:32
	v_log_f32_e32 v32, v32
	v_log_f32_e32 v33, v33
	v_pk_fma_f32 v[72:73], v[26:27], v[84:85], v[72:73] op_sel:[0,1,0] op_sel_hi:[1,1,1]
	v_pk_fma_f32 v[74:75], v[28:29], v[84:85], v[74:75] op_sel:[0,1,0] op_sel_hi:[1,1,1]
	ds_write_b128 v38, v[72:75] offset:64
	v_pk_fma_f32 v[76:77], v[30:31], v[84:85], v[76:77] op_sel:[0,1,0] op_sel_hi:[1,1,1]
	v_pk_fma_f32 v[78:79], v[32:33], v[84:85], v[78:79] op_sel:[0,1,0] op_sel_hi:[1,1,1]
	ds_write_b128 v38, v[76:79] offset:96
	ds_read_b128 v[18:21], v87
	ds_read_b128 v[22:25], v87 offset:1152
	ds_read_b128 v[26:29], v87 offset:2304
	ds_read_b128 v[30:33], v87 offset:3456
	s_waitcnt lgkmcnt(3)
	buffer_store_dwordx4 v[18:21], v36, s[8:11], 0 offen
	s_waitcnt lgkmcnt(2)
	buffer_store_dwordx4 v[22:25], v36, s[8:11], s24 offen
	s_waitcnt lgkmcnt(1)
	buffer_store_dwordx4 v[26:29], v36, s[8:11], s25 offen
	s_waitcnt lgkmcnt(0)
	buffer_store_dwordx4 v[30:33], v36, s[8:11], s26 offen
	s_endpgm

	.amdhsa_kernel _Z16sum_layer_kernelPKfS0_Pf
		.amdhsa_group_segment_fixed_size 51200
		.amdhsa_private_segment_fixed_size 0
		.amdhsa_kernarg_size 24
		.amdhsa_user_sgpr_count 2
		.amdhsa_user_sgpr_dispatch_ptr 0
		.amdhsa_user_sgpr_queue_ptr 0
		.amdhsa_user_sgpr_kernarg_segment_ptr 1
		.amdhsa_user_sgpr_dispatch_id 0
		.amdhsa_user_sgpr_kernarg_preload_length 0
		.amdhsa_user_sgpr_kernarg_preload_offset 0
		.amdhsa_user_sgpr_private_segment_size 0
		.amdhsa_uses_dynamic_stack 0
		.amdhsa_enable_private_segment 0
		.amdhsa_system_sgpr_workgroup_id_x 1
		.amdhsa_system_sgpr_workgroup_id_y 0
		.amdhsa_system_sgpr_workgroup_id_z 0
		.amdhsa_system_sgpr_workgroup_info 0
		.amdhsa_system_vgpr_workitem_id 0
		.amdhsa_next_free_vgpr 88
		.amdhsa_next_free_sgpr 56
		.amdhsa_accum_offset 88
		.amdhsa_reserve_vcc 1
		.amdhsa_float_round_mode_32 0
		.amdhsa_float_round_mode_16_64 0
		.amdhsa_float_denorm_mode_32 3
		.amdhsa_float_denorm_mode_16_64 3
		.amdhsa_dx10_clamp 1
		.amdhsa_ieee_mode 1
		.amdhsa_fp16_overflow 0
		.amdhsa_tg_split 0
		.amdhsa_exception_fp_ieee_invalid_op 0
		.amdhsa_exception_fp_denorm_src 0
		.amdhsa_exception_fp_ieee_div_zero 0
		.amdhsa_exception_fp_ieee_overflow 0
		.amdhsa_exception_fp_ieee_underflow 0
		.amdhsa_exception_fp_ieee_inexact 0
		.amdhsa_exception_int_div_zero 0
	.end_amdhsa_kernel

amdhsa.kernels:
  - .agpr_count:     0
    .args:
      - .address_space:  global
        .offset:         0
        .size:           8
        .value_kind:     global_buffer
      - .address_space:  global
        .offset:         8
        .size:           8
        .value_kind:     global_buffer
      - .address_space:  global
        .offset:         16
        .size:           8
        .value_kind:     global_buffer
    .group_segment_fixed_size: 51200
    .kernarg_segment_align: 8
    .kernarg_segment_size: 24
    .language:       OpenCL C
    .language_version:
      - 2
      - 0
    .max_flat_workgroup_size: 256
    .name:           _Z16sum_layer_kernelPKfS0_Pf
    .private_segment_fixed_size: 0
    .sgpr_count:     62
    .sgpr_spill_count: 0
    .symbol:         _Z16sum_layer_kernelPKfS0_Pf.kd
    .uniform_work_group_size: 1
    .uses_dynamic_stack: false
    .vgpr_count:     88
    .vgpr_spill_count: 0
    .wavefront_size: 64
